# speedup vs baseline: 1.0002x; 1.0002x over previous
_Z8knn_gemmPKcS0_Pi:
	s_ashr_i32 s3, s2, 31
	s_lshr_b32 s3, s3, 29
	s_add_i32 s3, s2, s3
	s_ashr_i32 s4, s3, 3
	s_and_b32 s3, s3, -8
	s_sub_i32 s3, s2, s3
	s_cmp_lt_i32 s3, 0
	s_movk_i32 s12, 0x188
	s_cselect_b32 s5, s12, 0x187
	s_mul_i32 s3, s5, s3
	s_add_i32 s3, s3, s4
	s_ashr_i32 s4, s3, 31
	s_lshr_b32 s4, s4, 27
	s_add_i32 s10, s3, s4
	s_ashr_i32 s4, s10, 5
	s_lshl_b32 s11, s4, 2
	s_sub_i32 s4, 0x187, s11
	s_min_i32 s13, s4, 4
	s_abs_i32 s14, s13
	v_cvt_f32_u32_e32 v1, s14
	s_andn2_b32 s10, s10, 31
	s_load_dwordx4 s[4:7], s[0:1], 0x0
	s_load_dwordx2 s[8:9], s[0:1], 0x10
	s_sub_i32 s0, s3, s10
	v_rcp_iflag_f32_e32 v1, v1
	s_sub_i32 s10, 0, s14
	s_abs_i32 s3, s0
	s_xor_b32 s1, s0, s13
	v_mul_f32_e32 v1, 0x4f7ffffe, v1
	v_cvt_u32_f32_e32 v1, v1
	s_ashr_i32 s1, s1, 31
	v_lshrrev_b32_e32 v2, 8, v0
	v_lshlrev_b32_e32 v168, 4, v0
	v_readfirstlane_b32 s15, v1
	s_mul_i32 s10, s10, s15
	s_mul_hi_u32 s10, s15, s10
	s_add_i32 s15, s15, s10
	s_mul_hi_u32 s10, s3, s15
	s_mul_i32 s15, s10, s14
	s_sub_i32 s3, s3, s15
	s_add_i32 s15, s10, 1
	s_sub_i32 s16, s3, s14
	s_cmp_ge_u32 s3, s14
	s_cselect_b32 s10, s15, s10
	s_cselect_b32 s3, s16, s3
	s_add_i32 s15, s10, 1
	s_cmp_ge_u32 s3, s14
	s_cselect_b32 s3, s15, s10
	s_xor_b32 s3, s3, s1
	s_sub_i32 s34, s3, s1
	s_mul_i32 s1, s34, s13
	s_sub_i32 s0, s0, s1
	s_add_i32 s11, s11, s0
	v_readfirstlane_b32 s1, v0
	s_sub_i32 s13, 0x186, s11
	s_lshl_b32 s3, s1, 4
	s_mul_i32 s10, s34, 0x30000
	s_mul_hi_i32 s1, s34, 0x30000
	s_waitcnt lgkmcnt(0)
	s_add_u32 s10, s6, s10
	s_addc_u32 s11, s7, s1
	s_mul_i32 s14, s13, 0x30000
	s_mul_hi_i32 s1, s13, 0x30000
	s_add_u32 s22, s4, s14
	v_readfirstlane_b32 s0, v2
	s_addc_u32 s23, s5, s1
	s_cmp_eq_u32 s0, 0
	s_cselect_b64 s[0:1], -1, 0
	s_add_u32 s16, s10, 0x2000
	s_addc_u32 s17, s11, 0
	s_add_u32 s18, s22, 0xfffff000
	s_addc_u32 s19, s23, -1
	s_and_b64 s[14:15], s[0:1], exec
	s_cselect_b32 s17, s17, s19
	s_cselect_b32 s16, s16, s18
	s_add_u32 s18, s22, 0x1000
	s_addc_u32 s19, s23, 0
	s_add_i32 s14, s3, 0
	s_mov_b64 s[20:21], s[10:11]
	s_add_i32 s15, s14, 0x2000
	v_lshrrev_b32_e32 v5, 2, v0
	v_lshrrev_b32_e32 v1, 4, v0
	s_add_i32 s16, s14, 0x4000
	v_and_b32_e32 v5, 2, v5
	s_add_u32 s18, s10, 0x3000
	s_addc_u32 s19, s11, 0
	s_add_u32 s3, s10, 0x5000
	s_addc_u32 s17, s11, 0
	s_add_u32 s20, s22, 0x2000
	s_addc_u32 s21, s23, 0
	s_and_b64 s[10:11], s[0:1], exec
	s_cselect_b32 s11, s17, s21
	s_cselect_b32 s10, s3, s20
	s_add_u32 s20, s22, 0x4000
	s_addc_u32 s21, s23, 0
	s_add_i32 s17, s14, 0x6000
	v_add_lshl_u32 v1, v5, v1, 3
	s_add_i32 s18, s14, 0x8000
	s_add_i32 s19, s14, 0xa000
	v_and_b32_e32 v3, 15, v0
	v_and_b32_e32 v5, 24, v1
	v_lshrrev_b32_e32 v1, 1, v0
	s_movk_i32 s3, 0x60
	s_add_i32 s20, s14, 0xc000
	v_and_or_b32 v1, v1, s3, v3
	v_lshl_or_b32 v2, v2, 6, v3
	s_add_u32 s21, s4, 0x12000
	v_and_b32_e32 v4, 48, v0
	v_mad_u32_u24 v6, v1, s3, 0
	v_mad_u32_u24 v2, v2, s3, 0
	s_addc_u32 s22, s5, 0
	v_add_u32_e32 v1, v6, v4
	v_add_u32_e32 v170, v2, v4
	v_add_u32_e32 v172, v6, v5
	v_add_u32_e32 v173, v2, v5
	v_mov_b32_e32 v39, 0
	s_add_u32 s23, s6, 0x12000
	v_add_u32_e32 v171, 0x3000, v170
	v_add_u32_e32 v174, 0x3040, v173
	v_mov_b32_e32 v169, v39
	v_add_u32_e32 v175, 0x12000, v1
	v_add_u32_e32 v176, 0x12040, v172
	v_add_u32_e32 v177, 0x15000, v170
	v_add_u32_e32 v178, 0x15040, v173
	v_add_u32_e32 v179, 0x12600, v1
	v_add_u32_e32 v180, 0x12640, v172
	v_add_u32_e32 v181, 0x15600, v170
	v_add_u32_e32 v182, 0x15640, v173
	v_add_u32_e32 v183, 0x15c00, v170
	v_add_u32_e32 v184, 0x15c40, v173
	v_add_u32_e32 v185, 0x16200, v170
	v_add_u32_e32 v186, 0x16240, v173
	s_addc_u32 s24, s7, 0
	v_mov_b32_e32 v187, 0x7f7f7f7f
	s_add_i32 s25, 0, 0x18000
	s_movk_i32 s26, 0xff80
	s_movk_i32 s27, 0x30e
	s_add_i32 s28, s14, 0xe000
	s_add_i32 s29, s20, 0x4000
	s_add_i32 s30, s14, 0x12000
	s_add_i32 s31, s14, 0x14000
	s_add_i32 s33, s14, 0x16000
	s_lshr_b32 s66, s14, 12
	s_and_b32 s54, s14, 0xfff
	s_mul_i32 s67, s66, 0x6000
	s_add_i32 s54, s54, s67
	s_add_i32 s55, s54, 0x1000
	s_add_i32 s56, s54, 0x2000
	s_add_i32 s57, s54, 0x3000
	s_add_i32 s58, s54, 0x4000
	s_add_i32 s59, s54, 0x5000
	s_add_i32 s60, s54, 0xc000
	s_add_i32 s61, s54, 0xd000
	s_add_i32 s62, s54, 0xe000
	s_add_i32 s63, s54, 0xf000
	s_add_i32 s64, s54, 0x10000
	s_add_i32 s65, s54, 0x11000
	v_and_b32_e32 v228, 0x3ff, v168
	s_lshr_b32 s74, s14, 11
	s_and_b32 s74, s74, 1
	s_lshr_b32 s75, s14, 10
	s_and_b32 s75, s75, 1
	s_mul_i32 s75, s75, 0x1800
	s_add_i32 s75, s75, 0xc00
	s_lshr_b32 s76, s14, 10
	s_and_b32 s76, s76, 3
	s_mul_i32 s76, s76, 0x1800
	s_add_i32 s76, s76, 0xc00
	s_mul_i32 s67, s66, 0x6000
	s_add_i32 s76, s76, s67
	s_add_i32 s77, s76, 0xc000
	v_add_u32_e32 v229, 0x1000, v228
	v_add_u32_e32 v230, 0x2000, v228
	s_mul_i32 s68, s34, 0x30000
	s_mul_hi_i32 s69, s34, 0x30000
	s_add_u32 s68, s6, s68
	s_addc_u32 s69, s7, s69
	s_mul_i32 s70, s13, 0x30000
	s_mul_hi_i32 s71, s13, 0x30000
	s_add_u32 s70, s4, s70
	s_addc_u32 s71, s5, s71
	s_mul_i32 s67, s66, 0x3000
	s_add_u32 s68, s68, s67
	s_addc_u32 s69, s69, 0
	s_add_u32 s70, s70, s67
	s_addc_u32 s71, s71, 0
	s_cmp_eq_u32 s74, 1
	s_cselect_b32 s68, s70, s68
	s_cselect_b32 s69, s71, s69
	s_add_u32 s68, s68, s75
	s_addc_u32 s69, s69, 0
	s_mov_b32 m0, s76
	s_nop 0
	global_load_lds_dwordx4 v228, s[68:69] offset:-3072
	global_load_lds_dwordx4 v228, s[68:69] offset:-2048
	global_load_lds_dwordx4 v228, s[68:69] offset:-1024
	global_load_lds_dwordx4 v228, s[68:69]
	global_load_lds_dwordx4 v228, s[68:69] offset:1024
	global_load_lds_dwordx4 v228, s[68:69] offset:2048
	s_waitcnt vmcnt(0)
	s_barrier
	s_add_u32 s68, s68, 0x6000
	s_addc_u32 s69, s69, 0
	s_add_u32 s70, s70, 0x6000
	s_addc_u32 s71, s71, 0
	s_mov_b32 m0, s77
	s_nop 0
	global_load_lds_dwordx4 v228, s[68:69] offset:-3072
	global_load_lds_dwordx4 v228, s[68:69] offset:-2048
	global_load_lds_dwordx4 v228, s[68:69] offset:-1024
	global_load_lds_dwordx4 v228, s[68:69]
	global_load_lds_dwordx4 v228, s[68:69] offset:1024
	global_load_lds_dwordx4 v228, s[68:69] offset:2048
	ds_read_b128 v[2:5], v170 offset:12288
	ds_read_b64 v[6:7], v173 offset:12352
	ds_read_b128 v[8:11], v170 offset:13824
	ds_read_b64 v[12:13], v173 offset:13888
	ds_read_b128 v[14:17], v170 offset:15360
	ds_read_b64 v[18:19], v173 offset:15424
	ds_read_b128 v[26:29], v170 offset:16896
	ds_read_b64 v[30:31], v173 offset:16960
	ds_read_b128 v[20:23], v1
	ds_read_b64 v[24:25], v172 offset:64
	ds_read_b128 v[32:35], v1 offset:1536
	ds_read_b64 v[36:37], v172 offset:1600
	s_cmp_eq_u32 s66, 1
	s_cbranch_scc0 .Lprio_skip
	s_setprio 1
.Lprio_skip:
	s_branch .LBB1_2
